# tail conversion v4: 4128 expert-weight items converted by idle CUs in dense GEMM, MoE GEMM2 and attention tail rounds
# speedup vs baseline: 1.0267x; 1.0049x over previous
.LBB0_55:
	s_cmp_lg_u32 s99, 0
	s_cbranch_scc1 .Ltc_itemdone
	v_readlane_b32 s2, v254, 0
	v_readlane_b32 s3, v254, 1
	s_load_dword s0, s[2:3], 0xe8
	s_add_i32 s14, s14, s15
	s_add_i32 s16, s16, s17
	s_add_i32 s10, s10, s18
	s_waitcnt lgkmcnt(0)
	s_add_i32 s22, s22, s0
	s_cmp_lt_i32 s22, 0x13e0
	s_cbranch_scc1 .Ltc_noskip
	s_cmp_ge_i32 s22, 0x2000
	s_cbranch_scc1 .Ltc_noskip
	s_and_b32 s22, s22, 0xff
	s_addk_i32 s22, 0x2000
	s_lshl_b32 s14, s22, 5
	s_lshl_b32 s16, s22, 4
	s_lshl_b32 s10, s22, 9

.Ltc_next:
	s_cmp_ge_u32 s100, 0x1020
	s_cbranch_scc1 .Ltc_alldone
	s_movk_i32 s0, 0x1fe0
	s_cmp_lt_u32 s100, 0xc20
	s_cselect_b32 s22, 0x13e0, s0
	s_add_i32 s22, s22, s100
	v_mbcnt_lo_u32_b32 v0, -1, 0
	v_mbcnt_hi_u32_b32 v0, -1, v0
	s_and_b32 s0, s94, 0xffffffc0
	s_nop 0
	v_ashrrev_i32_e32 v1, 31, v0
	v_add_u32_e32 v2, s0, v0
	s_movk_i32 s0, 0x44
	v_lshlrev_b32_e32 v5, 7, v0
	v_mul_lo_u32 v4, v0, s0
	v_mul_lo_u32 v12, v2, s0
	v_lshrrev_b32_e32 v3, 1, v2
	v_and_b32_e32 v5, 0x80, v5
	s_movk_i32 s0, 0x7f
	v_and_or_b32 v3, v3, s0, v5
	s_lshl_b32 s6, s95, 3
	s_add_u32 s7, s88, 0x22000000
	s_addc_u32 s11, s89, 0
	v_add_u32_e32 v4, 0, v4
	s_add_u32 s12, s88, 0x2000000
	v_add_u32_e32 v4, s6, v4
	s_mov_b32 s1, 0
	s_addc_u32 s13, s89, 0
	s_lshl_b32 s14, s22, 5
	s_lshl_b32 s16, s22, 4
	s_lshl_b32 s10, s22, 9
	s_mov_b32 s19, 0xc3e00000
	s_movk_i32 s20, 0xff
	v_add_u32_e32 v5, 0x1100, v4
	v_add_u32_e32 v6, 0x2200, v4
	v_add_u32_e32 v7, 0x3300, v4
	v_add_u32_e32 v8, 0x4400, v4
	v_add_u32_e32 v9, 0x5500, v4
	v_add_u32_e32 v10, 0x6600, v4
	v_add_u32_e32 v11, 0x7700, v4
	v_add_u32_e32 v12, 0, v12
	s_movk_i32 s21, 0xff00
	v_mov_b32_e32 v13, 0x43e00000
	v_mov_b32_e32 v14, 8
	s_branch .LBB0_56

.Ltc_alldone:
	s_cmp_eq_u32 s99, 1
	s_cbranch_scc1 .Ltc_ret_1
	s_cmp_eq_u32 s99, 2
	s_cbranch_scc1 .Ltc_ret_2
	s_cmp_eq_u32 s99, 3
	s_cbranch_scc1 .Ltc_ret_3
	s_cmp_eq_u32 s99, 4
	s_cbranch_scc1 .Ltc_ret_4
	s_cmp_eq_u32 s99, 5
	s_cbranch_scc1 .Ltc_ret_5
	s_cmp_eq_u32 s99, 6
	s_cbranch_scc1 .Ltc_ret_6
	s_branch .Ltc_s1_fwd

.LBB0_284:
	s_cmp_lt_u32 s96, 64
	s_cbranch_scc1 .Ltc_skip_2
	v_writelane_b32 v200, s0, 0
	s_nop 1
	v_writelane_b32 v200, s1, 1
	s_nop 1
	v_writelane_b32 v200, s2, 2
	s_nop 1
	v_writelane_b32 v200, s3, 3
	s_nop 1
	v_writelane_b32 v200, s4, 4
	s_nop 1
	v_writelane_b32 v200, s5, 5
	s_nop 1
	v_writelane_b32 v200, s6, 6
	s_nop 1
	v_writelane_b32 v200, s7, 7
	s_nop 1
	v_writelane_b32 v200, s10, 8
	s_nop 1
	v_writelane_b32 v200, s11, 9
	s_nop 1
	v_writelane_b32 v200, s12, 10
	s_nop 1
	v_writelane_b32 v200, s13, 11
	s_nop 1
	v_writelane_b32 v200, s14, 12
	s_nop 1
	v_writelane_b32 v200, s15, 13
	s_nop 1
	v_writelane_b32 v200, s16, 14
	s_nop 1
	v_writelane_b32 v200, s17, 15
	s_nop 1
	v_writelane_b32 v200, s18, 16
	s_nop 1
	v_writelane_b32 v200, s19, 17
	s_nop 1
	v_writelane_b32 v200, s20, 18
	s_nop 1
	v_writelane_b32 v200, s21, 19
	s_nop 1
	v_writelane_b32 v200, s22, 20
	s_nop 1
	v_writelane_b32 v200, s23, 21
	s_nop 1
	v_writelane_b32 v200, s24, 22
	s_nop 1
	v_writelane_b32 v200, s25, 23
	s_nop 1
	v_writelane_b32 v200, s36, 24
	s_nop 1
	v_writelane_b32 v200, s37, 25
	s_nop 1
	v_writelane_b32 v200, s38, 26
	s_nop 1
	v_writelane_b32 v200, s39, 27
	s_nop 1
	v_writelane_b32 v200, s40, 28
	s_nop 1
	v_writelane_b32 v200, s41, 29
	s_nop 1
	v_writelane_b32 v200, s42, 30
	s_nop 1
	v_writelane_b32 v200, s43, 31
	s_nop 1
	v_writelane_b32 v200, s44, 32
	s_nop 1
	v_writelane_b32 v200, s45, 33
	s_nop 1
	v_writelane_b32 v200, s46, 34
	s_nop 1
	v_writelane_b32 v200, s47, 35
	s_nop 1
	v_writelane_b32 v200, s48, 36
	s_nop 1
	v_writelane_b32 v200, s49, 37
	s_nop 1
	v_writelane_b32 v200, s50, 38
	s_nop 1
	v_writelane_b32 v200, s51, 39
	s_nop 1
	s_mov_b32 s99, 2
	s_mov_b32 s98, 1
	s_mov_b32 s101, 192
	s_add_i32 s100, s96, 384
	s_branch .Ltc_next
.Ltc_ret_2:
	s_mov_b32 s99, 0
	v_readlane_b32 s0, v200, 0
	v_readlane_b32 s1, v200, 1
	v_readlane_b32 s2, v200, 2
	v_readlane_b32 s3, v200, 3
	v_readlane_b32 s4, v200, 4
	v_readlane_b32 s5, v200, 5
	v_readlane_b32 s6, v200, 6
	v_readlane_b32 s7, v200, 7
	v_readlane_b32 s10, v200, 8
	v_readlane_b32 s11, v200, 9
	v_readlane_b32 s12, v200, 10
	v_readlane_b32 s13, v200, 11
	v_readlane_b32 s14, v200, 12
	v_readlane_b32 s15, v200, 13
	v_readlane_b32 s16, v200, 14
	v_readlane_b32 s17, v200, 15
	v_readlane_b32 s18, v200, 16
	v_readlane_b32 s19, v200, 17
	v_readlane_b32 s20, v200, 18
	v_readlane_b32 s21, v200, 19
	v_readlane_b32 s22, v200, 20
	v_readlane_b32 s23, v200, 21
	v_readlane_b32 s24, v200, 22
	v_readlane_b32 s25, v200, 23
	v_readlane_b32 s36, v200, 24
	v_readlane_b32 s37, v200, 25
	v_readlane_b32 s38, v200, 26
	v_readlane_b32 s39, v200, 27
	v_readlane_b32 s40, v200, 28
	v_readlane_b32 s41, v200, 29
	v_readlane_b32 s42, v200, 30
	v_readlane_b32 s43, v200, 31
	v_readlane_b32 s44, v200, 32
	v_readlane_b32 s45, v200, 33
	v_readlane_b32 s46, v200, 34
	v_readlane_b32 s47, v200, 35
	v_readlane_b32 s48, v200, 36
	v_readlane_b32 s49, v200, 37
	v_readlane_b32 s50, v200, 38
	v_readlane_b32 s51, v200, 39
	s_nop 1
.Ltc_skip_2:
	v_readlane_b32 s2, v254, 0
	v_readlane_b32 s3, v254, 1
	s_load_dwordx2 s[2:3], s[2:3], 0xd8
	s_waitcnt lgkmcnt(0)
	s_cmp_gt_i32 s3, 4
	s_cselect_b64 s[2:3], -1, 0
	s_and_b64 s[0:1], s[0:1], s[2:3]
	s_andn2_b64 vcc, exec, s[0:1]
	s_cbranch_vccnz .LBB0_340
	s_waitcnt vmcnt(0)
	s_cmp_gt_u32 s94, 63
	s_barrier
	s_cbranch_scc1 .LBB0_339
	v_mbcnt_lo_u32_b32 v0, -1, 0
	v_mbcnt_hi_u32_b32 v0, -1, v0
	v_cmp_eq_u32_e32 vcc, 0, v0
	s_and_saveexec_b64 s[0:1], vcc
	s_cbranch_execz .LBB0_338
	s_add_i32 s4, 0, 0x20020
	v_mov_b32_e32 v0, s4
	s_waitcnt vmcnt(0) expcnt(0) lgkmcnt(0)
	ds_read_b32 v2, v0
	s_add_i32 s4, 0, 0x20024
	v_mov_b32_e32 v0, s4
	ds_read_b32 v0, v0
	s_waitcnt lgkmcnt(1)
	v_cmp_ne_u32_e32 vcc, 0, v2
	s_cbranch_vccnz .LBB0_302
	v_readlane_b32 s4, v254, 2
	v_readlane_b32 s10, v254, 0
	v_readlane_b32 s5, v254, 3
	v_readlane_b32 s11, v254, 1
	s_load_dwordx2 s[8:9], s[4:5], 0x4
	s_mov_b32 s46, 1
	s_load_dword s10, s[10:11], 0xe8
	s_add_u32 s4, s88, 0x4200
	s_addc_u32 s5, s89, 0
	s_add_u32 s6, s88, 0x4400
	s_addc_u32 s7, s89, 0
	s_waitcnt lgkmcnt(0)
	s_mul_i32 s33, s8, s10
	s_add_u32 s8, s88, 0x4500
	s_mul_i32 s33, s33, s9
	s_addc_u32 s9, s89, 0
	s_add_u32 s10, s88, 0x4600
	s_addc_u32 s11, s89, 0
	s_add_u32 s12, s88, 0x4700
	s_addc_u32 s13, s89, 0
	s_add_u32 s14, s88, 0x4800
	s_addc_u32 s15, s89, 0
	s_add_u32 s16, s88, 0x4900
	s_addc_u32 s17, s89, 0
	s_add_u32 s18, s88, 0x4a00
	s_addc_u32 s19, s89, 0
	s_add_u32 s20, s88, 0x4b00
	s_addc_u32 s21, s89, 0
	s_add_u32 s22, s88, 0x4c00
	s_addc_u32 s23, s89, 0
	s_add_u32 s24, s88, 0x4d00
	s_addc_u32 s25, s89, 0
	s_add_u32 s26, s88, 0x4e00
	s_addc_u32 s27, s89, 0
	s_add_u32 s28, s88, 0x4f00
	s_addc_u32 s29, s89, 0
	s_add_u32 s30, s88, 0x5000
	s_addc_u32 s31, s89, 0
	s_add_u32 s34, s88, 0x5100
	s_addc_u32 s35, s89, 0
	s_add_u32 s36, s88, 0x5200
	s_addc_u32 s37, s89, 0
	s_add_u32 s38, s88, 0x5300
	s_addc_u32 s39, s89, 0
	v_mov_b32_e32 v16, 0
	s_branch .LBB0_290

.LBB0_359:
	s_cmp_lt_u32 s96, 32
	s_cbranch_scc1 .Ltc_skip_3
	v_writelane_b32 v200, s0, 0
	s_nop 1
	v_writelane_b32 v200, s1, 1
	s_nop 1
	v_writelane_b32 v200, s2, 2
	s_nop 1
	v_writelane_b32 v200, s3, 3
	s_nop 1
	v_writelane_b32 v200, s4, 4
	s_nop 1
	v_writelane_b32 v200, s5, 5
	s_nop 1
	v_writelane_b32 v200, s6, 6
	s_nop 1
	v_writelane_b32 v200, s7, 7
	s_nop 1
	v_writelane_b32 v200, s10, 8
	s_nop 1
	v_writelane_b32 v200, s11, 9
	s_nop 1
	v_writelane_b32 v200, s12, 10
	s_nop 1
	v_writelane_b32 v200, s13, 11
	s_nop 1
	v_writelane_b32 v200, s14, 12
	s_nop 1
	v_writelane_b32 v200, s15, 13
	s_nop 1
	v_writelane_b32 v200, s16, 14
	s_nop 1
	v_writelane_b32 v200, s17, 15
	s_nop 1
	v_writelane_b32 v200, s18, 16
	s_nop 1
	v_writelane_b32 v200, s19, 17
	s_nop 1
	v_writelane_b32 v200, s20, 18
	s_nop 1
	v_writelane_b32 v200, s21, 19
	s_nop 1
	v_writelane_b32 v200, s22, 20
	s_nop 1
	v_writelane_b32 v200, s23, 21
	s_nop 1
	v_writelane_b32 v200, s24, 22
	s_nop 1
	v_writelane_b32 v200, s25, 23
	s_nop 1
	v_writelane_b32 v200, s36, 24
	s_nop 1
	v_writelane_b32 v200, s37, 25
	s_nop 1
	v_writelane_b32 v200, s38, 26
	s_nop 1
	v_writelane_b32 v200, s39, 27
	s_nop 1
	v_writelane_b32 v200, s40, 28
	s_nop 1
	v_writelane_b32 v200, s41, 29
	s_nop 1
	v_writelane_b32 v200, s42, 30
	s_nop 1
	v_writelane_b32 v200, s43, 31
	s_nop 1
	v_writelane_b32 v200, s44, 32
	s_nop 1
	v_writelane_b32 v200, s45, 33
	s_nop 1
	v_writelane_b32 v200, s46, 34
	s_nop 1
	v_writelane_b32 v200, s47, 35
	s_nop 1
	v_writelane_b32 v200, s48, 36
	s_nop 1
	v_writelane_b32 v200, s49, 37
	s_nop 1
	v_writelane_b32 v200, s50, 38
	s_nop 1
	v_writelane_b32 v200, s51, 39
	s_nop 1
	s_mov_b32 s99, 3
	s_mov_b32 s98, 2
	s_mov_b32 s101, 224
	s_add_i32 s100, s96, 608
	s_branch .Ltc_next

.LBB0_668:
	s_cmp_lt_u32 s96, 144
	s_cbranch_scc1 .Ltc_skip_4
	v_writelane_b32 v200, s0, 0
	s_nop 1
	v_writelane_b32 v200, s1, 1
	s_nop 1
	v_writelane_b32 v200, s2, 2
	s_nop 1
	v_writelane_b32 v200, s3, 3
	s_nop 1
	v_writelane_b32 v200, s4, 4
	s_nop 1
	v_writelane_b32 v200, s5, 5
	s_nop 1
	v_writelane_b32 v200, s6, 6
	s_nop 1
	v_writelane_b32 v200, s7, 7
	s_nop 1
	v_writelane_b32 v200, s10, 8
	s_nop 1
	v_writelane_b32 v200, s11, 9
	s_nop 1
	v_writelane_b32 v200, s12, 10
	s_nop 1
	v_writelane_b32 v200, s13, 11
	s_nop 1
	v_writelane_b32 v200, s14, 12
	s_nop 1
	v_writelane_b32 v200, s15, 13
	s_nop 1
	v_writelane_b32 v200, s16, 14
	s_nop 1
	v_writelane_b32 v200, s17, 15
	s_nop 1
	v_writelane_b32 v200, s18, 16
	s_nop 1
	v_writelane_b32 v200, s19, 17
	s_nop 1
	v_writelane_b32 v200, s20, 18
	s_nop 1
	v_writelane_b32 v200, s21, 19
	s_nop 1
	v_writelane_b32 v200, s22, 20
	s_nop 1
	v_writelane_b32 v200, s23, 21
	s_nop 1
	v_writelane_b32 v200, s24, 22
	s_nop 1
	v_writelane_b32 v200, s25, 23
	s_nop 1
	v_writelane_b32 v200, s36, 24
	s_nop 1
	v_writelane_b32 v200, s37, 25
	s_nop 1
	v_writelane_b32 v200, s38, 26
	s_nop 1
	v_writelane_b32 v200, s39, 27
	s_nop 1
	v_writelane_b32 v200, s40, 28
	s_nop 1
	v_writelane_b32 v200, s41, 29
	s_nop 1
	v_writelane_b32 v200, s42, 30
	s_nop 1
	v_writelane_b32 v200, s43, 31
	s_nop 1
	v_writelane_b32 v200, s44, 32
	s_nop 1
	v_writelane_b32 v200, s45, 33
	s_nop 1
	v_writelane_b32 v200, s46, 34
	s_nop 1
	v_writelane_b32 v200, s47, 35
	s_nop 1
	v_writelane_b32 v200, s48, 36
	s_nop 1
	v_writelane_b32 v200, s49, 37
	s_nop 1
	v_writelane_b32 v200, s50, 38
	s_nop 1
	v_writelane_b32 v200, s51, 39
	s_nop 1
	s_mov_b32 s99, 4
	s_mov_b32 s98, 2
	s_mov_b32 s101, 112
	s_add_i32 s100, s96, 944
	s_branch .Ltc_next

.LBB0_807:
	s_cmp_lt_u32 s96, 48
	s_cbranch_scc1 .Ltc_skip_5
	v_writelane_b32 v200, s0, 0
	s_nop 1
	v_writelane_b32 v200, s1, 1
	s_nop 1
	v_writelane_b32 v200, s2, 2
	s_nop 1
	v_writelane_b32 v200, s3, 3
	s_nop 1
	v_writelane_b32 v200, s4, 4
	s_nop 1
	v_writelane_b32 v200, s5, 5
	s_nop 1
	v_writelane_b32 v200, s6, 6
	s_nop 1
	v_writelane_b32 v200, s7, 7
	s_nop 1
	v_writelane_b32 v200, s10, 8
	s_nop 1
	v_writelane_b32 v200, s11, 9
	s_nop 1
	v_writelane_b32 v200, s12, 10
	s_nop 1
	v_writelane_b32 v200, s13, 11
	s_nop 1
	v_writelane_b32 v200, s14, 12
	s_nop 1
	v_writelane_b32 v200, s15, 13
	s_nop 1
	v_writelane_b32 v200, s16, 14
	s_nop 1
	v_writelane_b32 v200, s17, 15
	s_nop 1
	v_writelane_b32 v200, s18, 16
	s_nop 1
	v_writelane_b32 v200, s19, 17
	s_nop 1
	v_writelane_b32 v200, s20, 18
	s_nop 1
	v_writelane_b32 v200, s21, 19
	s_nop 1
	v_writelane_b32 v200, s22, 20
	s_nop 1
	v_writelane_b32 v200, s23, 21
	s_nop 1
	v_writelane_b32 v200, s24, 22
	s_nop 1
	v_writelane_b32 v200, s25, 23
	s_nop 1
	v_writelane_b32 v200, s36, 24
	s_nop 1
	v_writelane_b32 v200, s37, 25
	s_nop 1
	v_writelane_b32 v200, s38, 26
	s_nop 1
	v_writelane_b32 v200, s39, 27
	s_nop 1
	v_writelane_b32 v200, s40, 28
	s_nop 1
	v_writelane_b32 v200, s41, 29
	s_nop 1
	v_writelane_b32 v200, s42, 30
	s_nop 1
	v_writelane_b32 v200, s43, 31
	s_nop 1
	v_writelane_b32 v200, s44, 32
	s_nop 1
	v_writelane_b32 v200, s45, 33
	s_nop 1
	v_writelane_b32 v200, s46, 34
	s_nop 1
	v_writelane_b32 v200, s47, 35
	s_nop 1
	v_writelane_b32 v200, s48, 36
	s_nop 1
	v_writelane_b32 v200, s49, 37
	s_nop 1
	v_writelane_b32 v200, s50, 38
	s_nop 1
	v_writelane_b32 v200, s51, 39
	s_nop 1
	s_mov_b32 s99, 5
	s_mov_b32 s98, 2
	s_mov_b32 s101, 208
	s_add_i32 s100, s96, 1264
	s_branch .Ltc_next

.Ltc_s1_fwd:
	s_cmp_eq_u32 s99, 7
	s_cbranch_scc1 .Ltc_ret_7
	s_cmp_eq_u32 s99, 8
	s_cbranch_scc1 .Ltc_ret_8
	s_cmp_eq_u32 s99, 9
	s_cbranch_scc1 .Ltc_ret_9
	s_cmp_eq_u32 s99, 10
	s_cbranch_scc1 .Ltc_ret_10
	s_branch .Ltc_s2_fwd

.LBB0_1052:
	s_cmp_lt_u32 s96, 32
	s_cbranch_scc1 .Ltc_skip_6
	v_writelane_b32 v200, s0, 0
	s_nop 1
	v_writelane_b32 v200, s1, 1
	s_nop 1
	v_writelane_b32 v200, s2, 2
	s_nop 1
	v_writelane_b32 v200, s3, 3
	s_nop 1
	v_writelane_b32 v200, s4, 4
	s_nop 1
	v_writelane_b32 v200, s5, 5
	s_nop 1
	v_writelane_b32 v200, s6, 6
	s_nop 1
	v_writelane_b32 v200, s7, 7
	s_nop 1
	v_writelane_b32 v200, s10, 8
	s_nop 1
	v_writelane_b32 v200, s11, 9
	s_nop 1
	v_writelane_b32 v200, s12, 10
	s_nop 1
	v_writelane_b32 v200, s13, 11
	s_nop 1
	v_writelane_b32 v200, s14, 12
	s_nop 1
	v_writelane_b32 v200, s15, 13
	s_nop 1
	v_writelane_b32 v200, s16, 14
	s_nop 1
	v_writelane_b32 v200, s17, 15
	s_nop 1
	v_writelane_b32 v200, s18, 16
	s_nop 1
	v_writelane_b32 v200, s19, 17
	s_nop 1
	v_writelane_b32 v200, s20, 18
	s_nop 1
	v_writelane_b32 v200, s21, 19
	s_nop 1
	v_writelane_b32 v200, s22, 20
	s_nop 1
	v_writelane_b32 v200, s23, 21
	s_nop 1
	v_writelane_b32 v200, s24, 22
	s_nop 1
	v_writelane_b32 v200, s25, 23
	s_nop 1
	v_writelane_b32 v200, s36, 24
	s_nop 1
	v_writelane_b32 v200, s37, 25
	s_nop 1
	v_writelane_b32 v200, s38, 26
	s_nop 1
	v_writelane_b32 v200, s39, 27
	s_nop 1
	v_writelane_b32 v200, s40, 28
	s_nop 1
	v_writelane_b32 v200, s41, 29
	s_nop 1
	v_writelane_b32 v200, s42, 30
	s_nop 1
	v_writelane_b32 v200, s43, 31
	s_nop 1
	v_writelane_b32 v200, s44, 32
	s_nop 1
	v_writelane_b32 v200, s45, 33
	s_nop 1
	v_writelane_b32 v200, s46, 34
	s_nop 1
	v_writelane_b32 v200, s47, 35
	s_nop 1
	v_writelane_b32 v200, s48, 36
	s_nop 1
	v_writelane_b32 v200, s49, 37
	s_nop 1
	v_writelane_b32 v200, s50, 38
	s_nop 1
	v_writelane_b32 v200, s51, 39
	s_nop 1
	s_mov_b32 s99, 6
	s_mov_b32 s98, 2
	s_mov_b32 s101, 224
	s_add_i32 s100, s96, 1696
	s_branch .Ltc_next

.LBB0_1361:
	s_cmp_lt_u32 s96, 144
	s_cbranch_scc1 .Ltc_skip_7
	v_writelane_b32 v200, s0, 0
	s_nop 1
	v_writelane_b32 v200, s1, 1
	s_nop 1
	v_writelane_b32 v200, s2, 2
	s_nop 1
	v_writelane_b32 v200, s3, 3
	s_nop 1
	v_writelane_b32 v200, s4, 4
	s_nop 1
	v_writelane_b32 v200, s5, 5
	s_nop 1
	v_writelane_b32 v200, s6, 6
	s_nop 1
	v_writelane_b32 v200, s7, 7
	s_nop 1
	v_writelane_b32 v200, s10, 8
	s_nop 1
	v_writelane_b32 v200, s11, 9
	s_nop 1
	v_writelane_b32 v200, s12, 10
	s_nop 1
	v_writelane_b32 v200, s13, 11
	s_nop 1
	v_writelane_b32 v200, s14, 12
	s_nop 1
	v_writelane_b32 v200, s15, 13
	s_nop 1
	v_writelane_b32 v200, s16, 14
	s_nop 1
	v_writelane_b32 v200, s17, 15
	s_nop 1
	v_writelane_b32 v200, s18, 16
	s_nop 1
	v_writelane_b32 v200, s19, 17
	s_nop 1
	v_writelane_b32 v200, s20, 18
	s_nop 1
	v_writelane_b32 v200, s21, 19
	s_nop 1
	v_writelane_b32 v200, s22, 20
	s_nop 1
	v_writelane_b32 v200, s23, 21
	s_nop 1
	v_writelane_b32 v200, s24, 22
	s_nop 1
	v_writelane_b32 v200, s25, 23
	s_nop 1
	v_writelane_b32 v200, s36, 24
	s_nop 1
	v_writelane_b32 v200, s37, 25
	s_nop 1
	v_writelane_b32 v200, s38, 26
	s_nop 1
	v_writelane_b32 v200, s39, 27
	s_nop 1
	v_writelane_b32 v200, s40, 28
	s_nop 1
	v_writelane_b32 v200, s41, 29
	s_nop 1
	v_writelane_b32 v200, s42, 30
	s_nop 1
	v_writelane_b32 v200, s43, 31
	s_nop 1
	v_writelane_b32 v200, s44, 32
	s_nop 1
	v_writelane_b32 v200, s45, 33
	s_nop 1
	v_writelane_b32 v200, s46, 34
	s_nop 1
	v_writelane_b32 v200, s47, 35
	s_nop 1
	v_writelane_b32 v200, s48, 36
	s_nop 1
	v_writelane_b32 v200, s49, 37
	s_nop 1
	v_writelane_b32 v200, s50, 38
	s_nop 1
	v_writelane_b32 v200, s51, 39
	s_nop 1
	s_mov_b32 s99, 7
	s_mov_b32 s98, 2
	s_mov_b32 s101, 112
	s_add_i32 s100, s96, 2032
	s_branch .Ltc_s1_back

.LBB0_1495:
	s_cmp_lt_u32 s96, 48
	s_cbranch_scc1 .Ltc_skip_8
	v_writelane_b32 v200, s0, 0
	s_nop 1
	v_writelane_b32 v200, s1, 1
	s_nop 1
	v_writelane_b32 v200, s2, 2
	s_nop 1
	v_writelane_b32 v200, s3, 3
	s_nop 1
	v_writelane_b32 v200, s4, 4
	s_nop 1
	v_writelane_b32 v200, s5, 5
	s_nop 1
	v_writelane_b32 v200, s6, 6
	s_nop 1
	v_writelane_b32 v200, s7, 7
	s_nop 1
	v_writelane_b32 v200, s10, 8
	s_nop 1
	v_writelane_b32 v200, s11, 9
	s_nop 1
	v_writelane_b32 v200, s12, 10
	s_nop 1
	v_writelane_b32 v200, s13, 11
	s_nop 1
	v_writelane_b32 v200, s14, 12
	s_nop 1
	v_writelane_b32 v200, s15, 13
	s_nop 1
	v_writelane_b32 v200, s16, 14
	s_nop 1
	v_writelane_b32 v200, s17, 15
	s_nop 1
	v_writelane_b32 v200, s18, 16
	s_nop 1
	v_writelane_b32 v200, s19, 17
	s_nop 1
	v_writelane_b32 v200, s20, 18
	s_nop 1
	v_writelane_b32 v200, s21, 19
	s_nop 1
	v_writelane_b32 v200, s22, 20
	s_nop 1
	v_writelane_b32 v200, s23, 21
	s_nop 1
	v_writelane_b32 v200, s24, 22
	s_nop 1
	v_writelane_b32 v200, s25, 23
	s_nop 1
	v_writelane_b32 v200, s36, 24
	s_nop 1
	v_writelane_b32 v200, s37, 25
	s_nop 1
	v_writelane_b32 v200, s38, 26
	s_nop 1
	v_writelane_b32 v200, s39, 27
	s_nop 1
	v_writelane_b32 v200, s40, 28
	s_nop 1
	v_writelane_b32 v200, s41, 29
	s_nop 1
	v_writelane_b32 v200, s42, 30
	s_nop 1
	v_writelane_b32 v200, s43, 31
	s_nop 1
	v_writelane_b32 v200, s44, 32
	s_nop 1
	v_writelane_b32 v200, s45, 33
	s_nop 1
	v_writelane_b32 v200, s46, 34
	s_nop 1
	v_writelane_b32 v200, s47, 35
	s_nop 1
	v_writelane_b32 v200, s48, 36
	s_nop 1
	v_writelane_b32 v200, s49, 37
	s_nop 1
	v_writelane_b32 v200, s50, 38
	s_nop 1
	v_writelane_b32 v200, s51, 39
	s_nop 1
	s_mov_b32 s99, 8
	s_mov_b32 s98, 2
	s_mov_b32 s101, 208
	s_add_i32 s100, s96, 2352
	s_branch .Ltc_s1_back

.LBB0_1636:
	s_cmp_lt_u32 s96, 64
	s_cbranch_scc1 .Ltc_skip_9
	v_writelane_b32 v200, s0, 0
	s_nop 1
	v_writelane_b32 v200, s1, 1
	s_nop 1
	v_writelane_b32 v200, s2, 2
	s_nop 1
	v_writelane_b32 v200, s3, 3
	s_nop 1
	v_writelane_b32 v200, s4, 4
	s_nop 1
	v_writelane_b32 v200, s5, 5
	s_nop 1
	v_writelane_b32 v200, s6, 6
	s_nop 1
	v_writelane_b32 v200, s7, 7
	s_nop 1
	v_writelane_b32 v200, s10, 8
	s_nop 1
	v_writelane_b32 v200, s11, 9
	s_nop 1
	v_writelane_b32 v200, s12, 10
	s_nop 1
	v_writelane_b32 v200, s13, 11
	s_nop 1
	v_writelane_b32 v200, s14, 12
	s_nop 1
	v_writelane_b32 v200, s15, 13
	s_nop 1
	v_writelane_b32 v200, s16, 14
	s_nop 1
	v_writelane_b32 v200, s17, 15
	s_nop 1
	v_writelane_b32 v200, s18, 16
	s_nop 1
	v_writelane_b32 v200, s19, 17
	s_nop 1
	v_writelane_b32 v200, s20, 18
	s_nop 1
	v_writelane_b32 v200, s21, 19
	s_nop 1
	v_writelane_b32 v200, s22, 20
	s_nop 1
	v_writelane_b32 v200, s23, 21
	s_nop 1
	v_writelane_b32 v200, s24, 22
	s_nop 1
	v_writelane_b32 v200, s25, 23
	s_nop 1
	v_writelane_b32 v200, s36, 24
	s_nop 1
	v_writelane_b32 v200, s37, 25
	s_nop 1
	v_writelane_b32 v200, s38, 26
	s_nop 1
	v_writelane_b32 v200, s39, 27
	s_nop 1
	v_writelane_b32 v200, s40, 28
	s_nop 1
	v_writelane_b32 v200, s41, 29
	s_nop 1
	v_writelane_b32 v200, s42, 30
	s_nop 1
	v_writelane_b32 v200, s43, 31
	s_nop 1
	v_writelane_b32 v200, s44, 32
	s_nop 1
	v_writelane_b32 v200, s45, 33
	s_nop 1
	v_writelane_b32 v200, s46, 34
	s_nop 1
	v_writelane_b32 v200, s47, 35
	s_nop 1
	v_writelane_b32 v200, s48, 36
	s_nop 1
	v_writelane_b32 v200, s49, 37
	s_nop 1
	v_writelane_b32 v200, s50, 38
	s_nop 1
	v_writelane_b32 v200, s51, 39
	s_nop 1
	s_mov_b32 s99, 9
	s_mov_b32 s98, 1
	s_mov_b32 s101, 192
	s_add_i32 s100, s96, 2752
	s_branch .Ltc_s1_back
.Ltc_ret_9:
	s_mov_b32 s99, 0
	v_readlane_b32 s0, v200, 0
	v_readlane_b32 s1, v200, 1
	v_readlane_b32 s2, v200, 2
	v_readlane_b32 s3, v200, 3
	v_readlane_b32 s4, v200, 4
	v_readlane_b32 s5, v200, 5
	v_readlane_b32 s6, v200, 6
	v_readlane_b32 s7, v200, 7
	v_readlane_b32 s10, v200, 8
	v_readlane_b32 s11, v200, 9
	v_readlane_b32 s12, v200, 10
	v_readlane_b32 s13, v200, 11
	v_readlane_b32 s14, v200, 12
	v_readlane_b32 s15, v200, 13
	v_readlane_b32 s16, v200, 14
	v_readlane_b32 s17, v200, 15
	v_readlane_b32 s18, v200, 16
	v_readlane_b32 s19, v200, 17
	v_readlane_b32 s20, v200, 18
	v_readlane_b32 s21, v200, 19
	v_readlane_b32 s22, v200, 20
	v_readlane_b32 s23, v200, 21
	v_readlane_b32 s24, v200, 22
	v_readlane_b32 s25, v200, 23
	v_readlane_b32 s36, v200, 24
	v_readlane_b32 s37, v200, 25
	v_readlane_b32 s38, v200, 26
	v_readlane_b32 s39, v200, 27
	v_readlane_b32 s40, v200, 28
	v_readlane_b32 s41, v200, 29
	v_readlane_b32 s42, v200, 30
	v_readlane_b32 s43, v200, 31
	v_readlane_b32 s44, v200, 32
	v_readlane_b32 s45, v200, 33
	v_readlane_b32 s46, v200, 34
	v_readlane_b32 s47, v200, 35
	v_readlane_b32 s48, v200, 36
	v_readlane_b32 s49, v200, 37
	v_readlane_b32 s50, v200, 38
	v_readlane_b32 s51, v200, 39
	s_nop 1
.Ltc_skip_9:
	v_readlane_b32 s0, v254, 0
	v_readlane_b32 s1, v254, 1
	s_load_dwordx2 s[0:1], s[0:1], 0xd8
	v_readlane_b32 s2, v255, 11
	v_readlane_b32 s3, v255, 12
	s_waitcnt lgkmcnt(0)
	s_cmp_gt_i32 s1, 19
	s_cselect_b64 s[0:1], -1, 0
	s_and_b64 s[2:3], s[2:3], s[0:1]
	s_andn2_b64 vcc, exec, s[2:3]
	s_cbranch_vccnz .LBB0_1692
	s_waitcnt vmcnt(0)
	s_cmp_gt_u32 s94, 63
	s_barrier
	s_cbranch_scc1 .LBB0_1691
	v_mbcnt_lo_u32_b32 v0, -1, 0
	v_mbcnt_hi_u32_b32 v0, -1, v0
	v_cmp_eq_u32_e32 vcc, 0, v0
	s_and_saveexec_b64 s[2:3], vcc
	s_cbranch_execz .LBB0_1690
	s_add_i32 s4, 0, 0x20020
	v_mov_b32_e32 v0, s4
	s_waitcnt vmcnt(0) expcnt(0) lgkmcnt(0)
	ds_read_b32 v2, v0
	s_add_i32 s4, 0, 0x20024
	v_mov_b32_e32 v0, s4
	ds_read_b32 v0, v0
	s_waitcnt lgkmcnt(1)
	v_cmp_ne_u32_e32 vcc, 0, v2
	s_cbranch_vccnz .LBB0_1654
	v_readlane_b32 s4, v254, 2
	v_readlane_b32 s10, v254, 0
	v_readlane_b32 s5, v254, 3
	v_readlane_b32 s11, v254, 1
	s_load_dwordx2 s[8:9], s[4:5], 0x4
	s_mov_b32 s46, 1
	s_load_dword s10, s[10:11], 0xe8
	s_add_u32 s4, s88, 0x4200
	s_addc_u32 s5, s89, 0
	s_add_u32 s6, s88, 0x4400
	s_addc_u32 s7, s89, 0
	s_waitcnt lgkmcnt(0)
	s_mul_i32 s33, s8, s10
	s_add_u32 s8, s88, 0x4500
	s_mul_i32 s33, s33, s9
	s_addc_u32 s9, s89, 0
	s_add_u32 s10, s88, 0x4600
	s_addc_u32 s11, s89, 0
	s_add_u32 s12, s88, 0x4700
	s_addc_u32 s13, s89, 0
	s_add_u32 s14, s88, 0x4800
	s_addc_u32 s15, s89, 0
	s_add_u32 s16, s88, 0x4900
	s_addc_u32 s17, s89, 0
	s_add_u32 s18, s88, 0x4a00
	s_addc_u32 s19, s89, 0
	s_add_u32 s20, s88, 0x4b00
	s_addc_u32 s21, s89, 0
	s_add_u32 s22, s88, 0x4c00
	s_addc_u32 s23, s89, 0
	s_add_u32 s24, s88, 0x4d00
	s_addc_u32 s25, s89, 0
	s_add_u32 s26, s88, 0x4e00
	s_addc_u32 s27, s89, 0
	s_add_u32 s28, s88, 0x4f00
	s_addc_u32 s29, s89, 0
	s_add_u32 s30, s88, 0x5000
	s_addc_u32 s31, s89, 0
	s_add_u32 s34, s88, 0x5100
	s_addc_u32 s35, s89, 0
	s_add_u32 s36, s88, 0x5200
	s_addc_u32 s37, s89, 0
	s_add_u32 s38, s88, 0x5300
	s_addc_u32 s39, s89, 0
	v_mov_b32_e32 v16, 0
	s_branch .LBB0_1642

.LBB0_1711:
	s_cmp_lt_u32 s96, 32
	s_cbranch_scc1 .Ltc_skip_10
	v_writelane_b32 v200, s0, 0
	s_nop 1
	v_writelane_b32 v200, s1, 1
	s_nop 1
	v_writelane_b32 v200, s2, 2
	s_nop 1
	v_writelane_b32 v200, s3, 3
	s_nop 1
	v_writelane_b32 v200, s4, 4
	s_nop 1
	v_writelane_b32 v200, s5, 5
	s_nop 1
	v_writelane_b32 v200, s6, 6
	s_nop 1
	v_writelane_b32 v200, s7, 7
	s_nop 1
	v_writelane_b32 v200, s10, 8
	s_nop 1
	v_writelane_b32 v200, s11, 9
	s_nop 1
	v_writelane_b32 v200, s12, 10
	s_nop 1
	v_writelane_b32 v200, s13, 11
	s_nop 1
	v_writelane_b32 v200, s14, 12
	s_nop 1
	v_writelane_b32 v200, s15, 13
	s_nop 1
	v_writelane_b32 v200, s16, 14
	s_nop 1
	v_writelane_b32 v200, s17, 15
	s_nop 1
	v_writelane_b32 v200, s18, 16
	s_nop 1
	v_writelane_b32 v200, s19, 17
	s_nop 1
	v_writelane_b32 v200, s20, 18
	s_nop 1
	v_writelane_b32 v200, s21, 19
	s_nop 1
	v_writelane_b32 v200, s22, 20
	s_nop 1
	v_writelane_b32 v200, s23, 21
	s_nop 1
	v_writelane_b32 v200, s24, 22
	s_nop 1
	v_writelane_b32 v200, s25, 23
	s_nop 1
	v_writelane_b32 v200, s36, 24
	s_nop 1
	v_writelane_b32 v200, s37, 25
	s_nop 1
	v_writelane_b32 v200, s38, 26
	s_nop 1
	v_writelane_b32 v200, s39, 27
	s_nop 1
	v_writelane_b32 v200, s40, 28
	s_nop 1
	v_writelane_b32 v200, s41, 29
	s_nop 1
	v_writelane_b32 v200, s42, 30
	s_nop 1
	v_writelane_b32 v200, s43, 31
	s_nop 1
	v_writelane_b32 v200, s44, 32
	s_nop 1
	v_writelane_b32 v200, s45, 33
	s_nop 1
	v_writelane_b32 v200, s46, 34
	s_nop 1
	v_writelane_b32 v200, s47, 35
	s_nop 1
	v_writelane_b32 v200, s48, 36
	s_nop 1
	v_writelane_b32 v200, s49, 37
	s_nop 1
	v_writelane_b32 v200, s50, 38
	s_nop 1
	v_writelane_b32 v200, s51, 39
	s_nop 1
	s_mov_b32 s99, 10
	s_mov_b32 s98, 2
	s_mov_b32 s101, 224
	s_add_i32 s100, s96, 2976
	s_branch .Ltc_s1_back

.Ltc_s2_fwd:
	s_cmp_eq_u32 s99, 11
	s_cbranch_scc1 .Ltc_ret_11
	s_branch .Ltc_ret_12

.LBB0_2020:
	s_cmp_lt_u32 s96, 144
	s_cbranch_scc1 .Ltc_skip_11
	v_writelane_b32 v200, s0, 0
	s_nop 1
	v_writelane_b32 v200, s1, 1
	s_nop 1
	v_writelane_b32 v200, s2, 2
	s_nop 1
	v_writelane_b32 v200, s3, 3
	s_nop 1
	v_writelane_b32 v200, s4, 4
	s_nop 1
	v_writelane_b32 v200, s5, 5
	s_nop 1
	v_writelane_b32 v200, s6, 6
	s_nop 1
	v_writelane_b32 v200, s7, 7
	s_nop 1
	v_writelane_b32 v200, s10, 8
	s_nop 1
	v_writelane_b32 v200, s11, 9
	s_nop 1
	v_writelane_b32 v200, s12, 10
	s_nop 1
	v_writelane_b32 v200, s13, 11
	s_nop 1
	v_writelane_b32 v200, s14, 12
	s_nop 1
	v_writelane_b32 v200, s15, 13
	s_nop 1
	v_writelane_b32 v200, s16, 14
	s_nop 1
	v_writelane_b32 v200, s17, 15
	s_nop 1
	v_writelane_b32 v200, s18, 16
	s_nop 1
	v_writelane_b32 v200, s19, 17
	s_nop 1
	v_writelane_b32 v200, s20, 18
	s_nop 1
	v_writelane_b32 v200, s21, 19
	s_nop 1
	v_writelane_b32 v200, s22, 20
	s_nop 1
	v_writelane_b32 v200, s23, 21
	s_nop 1
	v_writelane_b32 v200, s24, 22
	s_nop 1
	v_writelane_b32 v200, s25, 23
	s_nop 1
	v_writelane_b32 v200, s36, 24
	s_nop 1
	v_writelane_b32 v200, s37, 25
	s_nop 1
	v_writelane_b32 v200, s38, 26
	s_nop 1
	v_writelane_b32 v200, s39, 27
	s_nop 1
	v_writelane_b32 v200, s40, 28
	s_nop 1
	v_writelane_b32 v200, s41, 29
	s_nop 1
	v_writelane_b32 v200, s42, 30
	s_nop 1
	v_writelane_b32 v200, s43, 31
	s_nop 1
	v_writelane_b32 v200, s44, 32
	s_nop 1
	v_writelane_b32 v200, s45, 33
	s_nop 1
	v_writelane_b32 v200, s46, 34
	s_nop 1
	v_writelane_b32 v200, s47, 35
	s_nop 1
	v_writelane_b32 v200, s48, 36
	s_nop 1
	v_writelane_b32 v200, s49, 37
	s_nop 1
	v_writelane_b32 v200, s50, 38
	s_nop 1
	v_writelane_b32 v200, s51, 39
	s_nop 1
	s_mov_b32 s99, 11
	s_mov_b32 s98, 2
	s_mov_b32 s101, 112
	s_add_i32 s100, s96, 3312
	s_branch .Ltc_s2_back

.LBB0_2154:
	s_cmp_lt_u32 s96, 32
	s_cbranch_scc1 .Ltc_skip_12
	v_writelane_b32 v200, s0, 0
	s_nop 1
	v_writelane_b32 v200, s1, 1
	s_nop 1
	v_writelane_b32 v200, s2, 2
	s_nop 1
	v_writelane_b32 v200, s3, 3
	s_nop 1
	v_writelane_b32 v200, s4, 4
	s_nop 1
	v_writelane_b32 v200, s5, 5
	s_nop 1
	v_writelane_b32 v200, s6, 6
	s_nop 1
	v_writelane_b32 v200, s7, 7
	s_nop 1
	v_writelane_b32 v200, s10, 8
	s_nop 1
	v_writelane_b32 v200, s11, 9
	s_nop 1
	v_writelane_b32 v200, s12, 10
	s_nop 1
	v_writelane_b32 v200, s13, 11
	s_nop 1
	v_writelane_b32 v200, s14, 12
	s_nop 1
	v_writelane_b32 v200, s15, 13
	s_nop 1
	v_writelane_b32 v200, s16, 14
	s_nop 1
	v_writelane_b32 v200, s17, 15
	s_nop 1
	v_writelane_b32 v200, s18, 16
	s_nop 1
	v_writelane_b32 v200, s19, 17
	s_nop 1
	v_writelane_b32 v200, s20, 18
	s_nop 1
	v_writelane_b32 v200, s21, 19
	s_nop 1
	v_writelane_b32 v200, s22, 20
	s_nop 1
	v_writelane_b32 v200, s23, 21
	s_nop 1
	v_writelane_b32 v200, s24, 22
	s_nop 1
	v_writelane_b32 v200, s25, 23
	s_nop 1
	v_writelane_b32 v200, s36, 24
	s_nop 1
	v_writelane_b32 v200, s37, 25
	s_nop 1
	v_writelane_b32 v200, s38, 26
	s_nop 1
	v_writelane_b32 v200, s39, 27
	s_nop 1
	v_writelane_b32 v200, s40, 28
	s_nop 1
	v_writelane_b32 v200, s41, 29
	s_nop 1
	v_writelane_b32 v200, s42, 30
	s_nop 1
	v_writelane_b32 v200, s43, 31
	s_nop 1
	v_writelane_b32 v200, s44, 32
	s_nop 1
	v_writelane_b32 v200, s45, 33
	s_nop 1
	v_writelane_b32 v200, s46, 34
	s_nop 1
	v_writelane_b32 v200, s47, 35
	s_nop 1
	v_writelane_b32 v200, s48, 36
	s_nop 1
	v_writelane_b32 v200, s49, 37
	s_nop 1
	v_writelane_b32 v200, s50, 38
	s_nop 1
	v_writelane_b32 v200, s51, 39
	s_nop 1
	s_mov_b32 s99, 12
	s_mov_b32 s98, 2
	s_mov_b32 s101, 224
	s_add_i32 s100, s96, 3648
	s_branch .Ltc_s2_back
